# baseline (speedup 1.0000x reference)
.LBB5_12:
	s_or_b64 exec, exec, s[0:1]
	s_lshl_b32 s0, s42, 9
	s_ashr_i32 s1, s0, 31
	s_lshl_b64 s[0:1], s[0:1], 2
	s_add_u32 s0, s24, s0
	s_addc_u32 s1, s25, s1
	s_lshl_b32 s2, s7, 2
	v_bfe_u32 v153, v0, 6, 2
	s_add_u32 s0, s0, s2
	s_addc_u32 s1, s1, 0
	v_lshlrev_b32_e32 v148, 7, v153
	v_mov_b32_e32 v149, 0
	v_lshl_add_u64 v[10:11], s[0:1], 0, v[148:149]
	v_mov_b32_e32 v147, v149
	v_lshl_add_u64 v[10:11], v[10:11], 0, v[146:147]
	v_and_b32_e32 v254, 48, v0
	v_lshl_add_u32 v254, v153, 7, v254
	v_add_u32_e32 v254, 0x22240, v254
	ds_read_b128 v[34:37], v254
	ds_read_b128 v[26:29], v254 offset:64
	ds_read_b128 v[18:21], v254 offset:512
	ds_read_b128 v[10:13], v254 offset:576
	s_ashr_i32 s35, s34, 31
	s_and_b32 s50, s59, 6
	s_lshl_b64 s[2:3], s[34:35], 3
	s_or_b32 s7, s2, s50
	s_or_b32 s2, s7, s58
	s_lshl_b64 s[24:25], s[2:3], 16
	v_lshrrev_b32_e32 v187, 6, v0
	s_add_u32 s28, s26, s24
	v_and_b32_e32 v157, 4, v187
	s_addc_u32 s29, s27, s25
	s_lshl_b32 s2, s58, 3
	v_lshlrev_b32_e32 v147, 6, v188
	v_lshrrev_b32_e32 v148, 1, v0
	v_lshlrev_b32_e32 v154, 10, v153
	v_lshlrev_b32_e32 v158, 13, v157
	s_cmp_lg_u32 s58, 0
	v_lshl_or_b32 v159, v157, 4, s2
	v_and_or_b32 v155, v148, 24, v147
	v_or_b32_e32 v148, v154, v158
	s_cselect_b64 s[24:25], -1, 0
	v_or_b32_e32 v156, v153, v159
	s_mov_b64 s[0:1], -1
	v_lshl_add_u64 v[150:151], s[28:29], 0, v[148:149]
	v_or_b32_e32 v148, v155, v152
	v_lshl_add_u32 v156, v156, 10, 0
	s_and_b64 vcc, exec, s[24:25]
	s_waitcnt vmcnt(0) lgkmcnt(0)
	s_barrier
	v_and_b32_e32 v216, 15, v0
	v_bfe_u32 v217, v0, 4, 2
	v_lshlrev_b32_e32 v218, 6, v216
	v_lshl_add_u32 v218, v217, 3, v218
	v_lshlrev_b32_e32 v219, 2, v216
	v_and_b32_e32 v219, 32, v219
	v_xor_b32_e32 v218, v218, v219
	v_bfe_u32 v219, v0, 6, 2
	v_lshl_add_u32 v218, v219, 10, v218
	v_lshrrev_b32_e32 v219, 8, v0
	v_lshl_add_u32 v216, v219, 16, v218
	s_lshl_b32 s96, s58, 13
	v_add_u32_e32 v216, s96, v216
	v_xor_b32_e32 v217, 32, v216
	v_lshl_add_u32 v218, v219, 15, v218
	v_xor_b32_e32 v219, 32, v218
	v_mov_b32_e32 v220, 0x3c800000
	v_mov_b32_e32 v221, 0x3c800000
	s_cmp_eq_u32 s58, 0
	s_cbranch_scc1 .Lep_pn0
	v_pk_fma_f32 v[142:143], v[142:143], v[220:221], v[34:35]
	v_pk_fma_f32 v[144:145], v[144:145], v[220:221], v[36:37]
	v_max_f32_e32 v142, 0, v142
	v_max_f32_e32 v143, 0, v143
	v_max_f32_e32 v144, 0, v144
	v_max_f32_e32 v145, 0, v145
	v_cvt_pk_f16_f32 v222, v142, v143
	v_cvt_pk_f16_f32 v223, v144, v145
	s_add_u32 s96, s28, 0x0
	s_addc_u32 s97, s29, 0
	global_store_dwordx2 v218, v[222:223], s[96:97] sc1
	v_pk_fma_f32 v[138:139], v[138:139], v[220:221], v[26:27]
	v_pk_fma_f32 v[140:141], v[140:141], v[220:221], v[28:29]
	v_max_f32_e32 v138, 0, v138
	v_max_f32_e32 v139, 0, v139
	v_max_f32_e32 v140, 0, v140
	v_max_f32_e32 v141, 0, v141
	v_cvt_pk_f16_f32 v224, v138, v139
	v_cvt_pk_f16_f32 v225, v140, v141
	global_store_dwordx2 v219, v[224:225], s[96:97] sc1
	v_pk_fma_f32 v[134:135], v[134:135], v[220:221], v[18:19]
	v_pk_fma_f32 v[136:137], v[136:137], v[220:221], v[20:21]
	v_max_f32_e32 v134, 0, v134
	v_max_f32_e32 v135, 0, v135
	v_max_f32_e32 v136, 0, v136
	v_max_f32_e32 v137, 0, v137
	v_cvt_pk_f16_f32 v222, v134, v135
	v_cvt_pk_f16_f32 v223, v136, v137
	s_add_u32 s96, s28, 0x1000
	s_addc_u32 s97, s29, 0
	global_store_dwordx2 v218, v[222:223], s[96:97] sc1
	v_pk_fma_f32 v[130:131], v[130:131], v[220:221], v[10:11]
	v_pk_fma_f32 v[132:133], v[132:133], v[220:221], v[12:13]
	v_max_f32_e32 v130, 0, v130
	v_max_f32_e32 v131, 0, v131
	v_max_f32_e32 v132, 0, v132
	v_max_f32_e32 v133, 0, v133
	v_cvt_pk_f16_f32 v224, v130, v131
	v_cvt_pk_f16_f32 v225, v132, v133
	global_store_dwordx2 v219, v[224:225], s[96:97] sc1
	v_pk_fma_f32 v[126:127], v[126:127], v[220:221], v[34:35]
	v_pk_fma_f32 v[128:129], v[128:129], v[220:221], v[36:37]
	v_max_f32_e32 v126, 0, v126
	v_max_f32_e32 v127, 0, v127
	v_max_f32_e32 v128, 0, v128
	v_max_f32_e32 v129, 0, v129
	v_cvt_pk_f16_f32 v222, v126, v127
	v_cvt_pk_f16_f32 v223, v128, v129
	s_add_u32 s96, s28, 0x2000
	s_addc_u32 s97, s29, 0
	global_store_dwordx2 v218, v[222:223], s[96:97] sc1
	v_pk_fma_f32 v[122:123], v[122:123], v[220:221], v[26:27]
	v_pk_fma_f32 v[124:125], v[124:125], v[220:221], v[28:29]
	v_max_f32_e32 v122, 0, v122
	v_max_f32_e32 v123, 0, v123
	v_max_f32_e32 v124, 0, v124
	v_max_f32_e32 v125, 0, v125
	v_cvt_pk_f16_f32 v224, v122, v123
	v_cvt_pk_f16_f32 v225, v124, v125
	global_store_dwordx2 v219, v[224:225], s[96:97] sc1
	v_pk_fma_f32 v[118:119], v[118:119], v[220:221], v[18:19]
	v_pk_fma_f32 v[120:121], v[120:121], v[220:221], v[20:21]
	v_max_f32_e32 v118, 0, v118
	v_max_f32_e32 v119, 0, v119
	v_max_f32_e32 v120, 0, v120
	v_max_f32_e32 v121, 0, v121
	v_cvt_pk_f16_f32 v222, v118, v119
	v_cvt_pk_f16_f32 v223, v120, v121
	s_add_u32 s96, s28, 0x3000
	s_addc_u32 s97, s29, 0
	global_store_dwordx2 v218, v[222:223], s[96:97] sc1
	v_pk_fma_f32 v[114:115], v[114:115], v[220:221], v[10:11]
	v_pk_fma_f32 v[116:117], v[116:117], v[220:221], v[12:13]
	v_max_f32_e32 v114, 0, v114
	v_max_f32_e32 v115, 0, v115
	v_max_f32_e32 v116, 0, v116
	v_max_f32_e32 v117, 0, v117
	v_cvt_pk_f16_f32 v224, v114, v115
	v_cvt_pk_f16_f32 v225, v116, v117
	global_store_dwordx2 v219, v[224:225], s[96:97] sc1
	v_pk_fma_f32 v[110:111], v[110:111], v[220:221], v[34:35]
	v_pk_fma_f32 v[112:113], v[112:113], v[220:221], v[36:37]
	v_max_f32_e32 v110, 0, v110
	v_max_f32_e32 v111, 0, v111
	v_max_f32_e32 v112, 0, v112
	v_max_f32_e32 v113, 0, v113
	v_cvt_pk_f16_f32 v222, v110, v111
	v_cvt_pk_f16_f32 v223, v112, v113
	s_add_u32 s96, s28, 0x4000
	s_addc_u32 s97, s29, 0
	global_store_dwordx2 v218, v[222:223], s[96:97] sc1
	v_pk_fma_f32 v[106:107], v[106:107], v[220:221], v[26:27]
	v_pk_fma_f32 v[108:109], v[108:109], v[220:221], v[28:29]
	v_max_f32_e32 v106, 0, v106
	v_max_f32_e32 v107, 0, v107
	v_max_f32_e32 v108, 0, v108
	v_max_f32_e32 v109, 0, v109
	v_cvt_pk_f16_f32 v224, v106, v107
	v_cvt_pk_f16_f32 v225, v108, v109
	global_store_dwordx2 v219, v[224:225], s[96:97] sc1
	v_pk_fma_f32 v[102:103], v[102:103], v[220:221], v[18:19]
	v_pk_fma_f32 v[104:105], v[104:105], v[220:221], v[20:21]
	v_max_f32_e32 v102, 0, v102
	v_max_f32_e32 v103, 0, v103
	v_max_f32_e32 v104, 0, v104
	v_max_f32_e32 v105, 0, v105
	v_cvt_pk_f16_f32 v222, v102, v103
	v_cvt_pk_f16_f32 v223, v104, v105
	s_add_u32 s96, s28, 0x5000
	s_addc_u32 s97, s29, 0
	global_store_dwordx2 v218, v[222:223], s[96:97] sc1
	v_pk_fma_f32 v[98:99], v[98:99], v[220:221], v[10:11]
	v_pk_fma_f32 v[100:101], v[100:101], v[220:221], v[12:13]
	v_max_f32_e32 v98, 0, v98
	v_max_f32_e32 v99, 0, v99
	v_max_f32_e32 v100, 0, v100
	v_max_f32_e32 v101, 0, v101
	v_cvt_pk_f16_f32 v224, v98, v99
	v_cvt_pk_f16_f32 v225, v100, v101
	global_store_dwordx2 v219, v[224:225], s[96:97] sc1
	v_pk_fma_f32 v[94:95], v[94:95], v[220:221], v[34:35]
	v_pk_fma_f32 v[96:97], v[96:97], v[220:221], v[36:37]
	v_max_f32_e32 v94, 0, v94
	v_max_f32_e32 v95, 0, v95
	v_max_f32_e32 v96, 0, v96
	v_max_f32_e32 v97, 0, v97
	v_cvt_pk_f16_f32 v222, v94, v95
	v_cvt_pk_f16_f32 v223, v96, v97
	s_add_u32 s96, s28, 0x6000
	s_addc_u32 s97, s29, 0
	global_store_dwordx2 v218, v[222:223], s[96:97] sc1
	v_pk_fma_f32 v[90:91], v[90:91], v[220:221], v[26:27]
	v_pk_fma_f32 v[92:93], v[92:93], v[220:221], v[28:29]
	v_max_f32_e32 v90, 0, v90
	v_max_f32_e32 v91, 0, v91
	v_max_f32_e32 v92, 0, v92
	v_max_f32_e32 v93, 0, v93
	v_cvt_pk_f16_f32 v224, v90, v91
	v_cvt_pk_f16_f32 v225, v92, v93
	global_store_dwordx2 v219, v[224:225], s[96:97] sc1
	v_pk_fma_f32 v[86:87], v[86:87], v[220:221], v[18:19]
	v_pk_fma_f32 v[88:89], v[88:89], v[220:221], v[20:21]
	v_max_f32_e32 v86, 0, v86
	v_max_f32_e32 v87, 0, v87
	v_max_f32_e32 v88, 0, v88
	v_max_f32_e32 v89, 0, v89
	v_cvt_pk_f16_f32 v222, v86, v87
	v_cvt_pk_f16_f32 v223, v88, v89
	s_add_u32 s96, s28, 0x7000
	s_addc_u32 s97, s29, 0
	global_store_dwordx2 v218, v[222:223], s[96:97] sc1
	v_pk_fma_f32 v[82:83], v[82:83], v[220:221], v[10:11]
	v_pk_fma_f32 v[84:85], v[84:85], v[220:221], v[12:13]
	v_max_f32_e32 v82, 0, v82
	v_max_f32_e32 v83, 0, v83
	v_max_f32_e32 v84, 0, v84
	v_max_f32_e32 v85, 0, v85
	v_cvt_pk_f16_f32 v224, v82, v83
	v_cvt_pk_f16_f32 v225, v84, v85
	global_store_dwordx2 v219, v[224:225], s[96:97] sc1
	v_pk_fma_f32 v[78:79], v[78:79], v[220:221], v[34:35]
	v_pk_fma_f32 v[80:81], v[80:81], v[220:221], v[36:37]
	v_max_f32_e32 v78, 0, v78
	v_max_f32_e32 v79, 0, v79
	v_max_f32_e32 v80, 0, v80
	v_max_f32_e32 v81, 0, v81
	v_cvt_pk_f16_f32 v222, v78, v79
	v_cvt_pk_f16_f32 v223, v80, v81
	ds_write_b64 v216, v[222:223] offset:0
	v_pk_fma_f32 v[74:75], v[74:75], v[220:221], v[26:27]
	v_pk_fma_f32 v[76:77], v[76:77], v[220:221], v[28:29]
	v_max_f32_e32 v74, 0, v74
	v_max_f32_e32 v75, 0, v75
	v_max_f32_e32 v76, 0, v76
	v_max_f32_e32 v77, 0, v77
	v_cvt_pk_f16_f32 v224, v74, v75
	v_cvt_pk_f16_f32 v225, v76, v77
	ds_write_b64 v217, v[224:225] offset:0
	v_pk_fma_f32 v[70:71], v[70:71], v[220:221], v[18:19]
	v_pk_fma_f32 v[72:73], v[72:73], v[220:221], v[20:21]
	v_max_f32_e32 v70, 0, v70
	v_max_f32_e32 v71, 0, v71
	v_max_f32_e32 v72, 0, v72
	v_max_f32_e32 v73, 0, v73
	v_cvt_pk_f16_f32 v222, v70, v71
	v_cvt_pk_f16_f32 v223, v72, v73
	ds_write_b64 v216, v[222:223] offset:4096
	v_pk_fma_f32 v[66:67], v[66:67], v[220:221], v[10:11]
	v_pk_fma_f32 v[68:69], v[68:69], v[220:221], v[12:13]
	v_max_f32_e32 v66, 0, v66
	v_max_f32_e32 v67, 0, v67
	v_max_f32_e32 v68, 0, v68
	v_max_f32_e32 v69, 0, v69
	v_cvt_pk_f16_f32 v224, v66, v67
	v_cvt_pk_f16_f32 v225, v68, v69
	ds_write_b64 v217, v[224:225] offset:4096
	v_pk_fma_f32 v[62:63], v[62:63], v[220:221], v[34:35]
	v_pk_fma_f32 v[64:65], v[64:65], v[220:221], v[36:37]
	v_max_f32_e32 v62, 0, v62
	v_max_f32_e32 v63, 0, v63
	v_max_f32_e32 v64, 0, v64
	v_max_f32_e32 v65, 0, v65
	v_cvt_pk_f16_f32 v222, v62, v63
	v_cvt_pk_f16_f32 v223, v64, v65
	ds_write_b64 v216, v[222:223] offset:16384
	v_pk_fma_f32 v[58:59], v[58:59], v[220:221], v[26:27]
	v_pk_fma_f32 v[60:61], v[60:61], v[220:221], v[28:29]
	v_max_f32_e32 v58, 0, v58
	v_max_f32_e32 v59, 0, v59
	v_max_f32_e32 v60, 0, v60
	v_max_f32_e32 v61, 0, v61
	v_cvt_pk_f16_f32 v224, v58, v59
	v_cvt_pk_f16_f32 v225, v60, v61
	ds_write_b64 v217, v[224:225] offset:16384
	v_pk_fma_f32 v[54:55], v[54:55], v[220:221], v[18:19]
	v_pk_fma_f32 v[56:57], v[56:57], v[220:221], v[20:21]
	v_max_f32_e32 v54, 0, v54
	v_max_f32_e32 v55, 0, v55
	v_max_f32_e32 v56, 0, v56
	v_max_f32_e32 v57, 0, v57
	v_cvt_pk_f16_f32 v222, v54, v55
	v_cvt_pk_f16_f32 v223, v56, v57
	ds_write_b64 v216, v[222:223] offset:20480
	v_pk_fma_f32 v[50:51], v[50:51], v[220:221], v[10:11]
	v_pk_fma_f32 v[52:53], v[52:53], v[220:221], v[12:13]
	v_max_f32_e32 v50, 0, v50
	v_max_f32_e32 v51, 0, v51
	v_max_f32_e32 v52, 0, v52
	v_max_f32_e32 v53, 0, v53
	v_cvt_pk_f16_f32 v224, v50, v51
	v_cvt_pk_f16_f32 v225, v52, v53
	ds_write_b64 v217, v[224:225] offset:20480
	v_pk_fma_f32 v[46:47], v[46:47], v[220:221], v[34:35]
	v_pk_fma_f32 v[48:49], v[48:49], v[220:221], v[36:37]
	v_max_f32_e32 v46, 0, v46
	v_max_f32_e32 v47, 0, v47
	v_max_f32_e32 v48, 0, v48
	v_max_f32_e32 v49, 0, v49
	v_cvt_pk_f16_f32 v222, v46, v47
	v_cvt_pk_f16_f32 v223, v48, v49
	ds_write_b64 v216, v[222:223] offset:32768
	v_pk_fma_f32 v[42:43], v[42:43], v[220:221], v[26:27]
	v_pk_fma_f32 v[44:45], v[44:45], v[220:221], v[28:29]
	v_max_f32_e32 v42, 0, v42
	v_max_f32_e32 v43, 0, v43
	v_max_f32_e32 v44, 0, v44
	v_max_f32_e32 v45, 0, v45
	v_cvt_pk_f16_f32 v224, v42, v43
	v_cvt_pk_f16_f32 v225, v44, v45
	ds_write_b64 v217, v[224:225] offset:32768
	v_pk_fma_f32 v[38:39], v[38:39], v[220:221], v[18:19]
	v_pk_fma_f32 v[40:41], v[40:41], v[220:221], v[20:21]
	v_max_f32_e32 v38, 0, v38
	v_max_f32_e32 v39, 0, v39
	v_max_f32_e32 v40, 0, v40
	v_max_f32_e32 v41, 0, v41
	v_cvt_pk_f16_f32 v222, v38, v39
	v_cvt_pk_f16_f32 v223, v40, v41
	ds_write_b64 v216, v[222:223] offset:36864
	v_pk_fma_f32 v[30:31], v[30:31], v[220:221], v[10:11]
	v_pk_fma_f32 v[32:33], v[32:33], v[220:221], v[12:13]
	v_max_f32_e32 v30, 0, v30
	v_max_f32_e32 v31, 0, v31
	v_max_f32_e32 v32, 0, v32
	v_max_f32_e32 v33, 0, v33
	v_cvt_pk_f16_f32 v224, v30, v31
	v_cvt_pk_f16_f32 v225, v32, v33
	ds_write_b64 v217, v[224:225] offset:36864
	v_pk_fma_f32 v[22:23], v[22:23], v[220:221], v[34:35]
	v_pk_fma_f32 v[24:25], v[24:25], v[220:221], v[36:37]
	v_max_f32_e32 v22, 0, v22
	v_max_f32_e32 v23, 0, v23
	v_max_f32_e32 v24, 0, v24
	v_max_f32_e32 v25, 0, v25
	v_cvt_pk_f16_f32 v222, v22, v23
	v_cvt_pk_f16_f32 v223, v24, v25
	ds_write_b64 v216, v[222:223] offset:49152
	v_pk_fma_f32 v[14:15], v[14:15], v[220:221], v[26:27]
	v_pk_fma_f32 v[16:17], v[16:17], v[220:221], v[28:29]
	v_max_f32_e32 v14, 0, v14
	v_max_f32_e32 v15, 0, v15
	v_max_f32_e32 v16, 0, v16
	v_max_f32_e32 v17, 0, v17
	v_cvt_pk_f16_f32 v224, v14, v15
	v_cvt_pk_f16_f32 v225, v16, v17
	ds_write_b64 v217, v[224:225] offset:49152
	v_pk_fma_f32 v[6:7], v[6:7], v[220:221], v[18:19]
	v_pk_fma_f32 v[8:9], v[8:9], v[220:221], v[20:21]
	v_max_f32_e32 v6, 0, v6
	v_max_f32_e32 v7, 0, v7
	v_max_f32_e32 v8, 0, v8
	v_max_f32_e32 v9, 0, v9
	v_cvt_pk_f16_f32 v222, v6, v7
	v_cvt_pk_f16_f32 v223, v8, v9
	ds_write_b64 v216, v[222:223] offset:53248
	v_pk_fma_f32 v[2:3], v[2:3], v[220:221], v[10:11]
	v_pk_fma_f32 v[4:5], v[4:5], v[220:221], v[12:13]
	v_max_f32_e32 v2, 0, v2
	v_max_f32_e32 v3, 0, v3
	v_max_f32_e32 v4, 0, v4
	v_max_f32_e32 v5, 0, v5
	v_cvt_pk_f16_f32 v224, v2, v3
	v_cvt_pk_f16_f32 v225, v4, v5
	ds_write_b64 v217, v[224:225] offset:53248
	s_branch .Lep_done
.Lep_pn0:
	v_pk_fma_f32 v[142:143], v[142:143], v[220:221], v[34:35]
	v_pk_fma_f32 v[144:145], v[144:145], v[220:221], v[36:37]
	v_max_f32_e32 v142, 0, v142
	v_max_f32_e32 v143, 0, v143
	v_max_f32_e32 v144, 0, v144
	v_max_f32_e32 v145, 0, v145
	v_cvt_pk_f16_f32 v222, v142, v143
	v_cvt_pk_f16_f32 v223, v144, v145
	ds_write_b64 v216, v[222:223] offset:0
	v_pk_fma_f32 v[138:139], v[138:139], v[220:221], v[26:27]
	v_pk_fma_f32 v[140:141], v[140:141], v[220:221], v[28:29]
	v_max_f32_e32 v138, 0, v138
	v_max_f32_e32 v139, 0, v139
	v_max_f32_e32 v140, 0, v140
	v_max_f32_e32 v141, 0, v141
	v_cvt_pk_f16_f32 v224, v138, v139
	v_cvt_pk_f16_f32 v225, v140, v141
	ds_write_b64 v217, v[224:225] offset:0
	v_pk_fma_f32 v[134:135], v[134:135], v[220:221], v[18:19]
	v_pk_fma_f32 v[136:137], v[136:137], v[220:221], v[20:21]
	v_max_f32_e32 v134, 0, v134
	v_max_f32_e32 v135, 0, v135
	v_max_f32_e32 v136, 0, v136
	v_max_f32_e32 v137, 0, v137
	v_cvt_pk_f16_f32 v222, v134, v135
	v_cvt_pk_f16_f32 v223, v136, v137
	ds_write_b64 v216, v[222:223] offset:4096
	v_pk_fma_f32 v[130:131], v[130:131], v[220:221], v[10:11]
	v_pk_fma_f32 v[132:133], v[132:133], v[220:221], v[12:13]
	v_max_f32_e32 v130, 0, v130
	v_max_f32_e32 v131, 0, v131
	v_max_f32_e32 v132, 0, v132
	v_max_f32_e32 v133, 0, v133
	v_cvt_pk_f16_f32 v224, v130, v131
	v_cvt_pk_f16_f32 v225, v132, v133
	ds_write_b64 v217, v[224:225] offset:4096
	v_pk_fma_f32 v[126:127], v[126:127], v[220:221], v[34:35]
	v_pk_fma_f32 v[128:129], v[128:129], v[220:221], v[36:37]
	v_max_f32_e32 v126, 0, v126
	v_max_f32_e32 v127, 0, v127
	v_max_f32_e32 v128, 0, v128
	v_max_f32_e32 v129, 0, v129
	v_cvt_pk_f16_f32 v222, v126, v127
	v_cvt_pk_f16_f32 v223, v128, v129
	ds_write_b64 v216, v[222:223] offset:16384
	v_pk_fma_f32 v[122:123], v[122:123], v[220:221], v[26:27]
	v_pk_fma_f32 v[124:125], v[124:125], v[220:221], v[28:29]
	v_max_f32_e32 v122, 0, v122
	v_max_f32_e32 v123, 0, v123
	v_max_f32_e32 v124, 0, v124
	v_max_f32_e32 v125, 0, v125
	v_cvt_pk_f16_f32 v224, v122, v123
	v_cvt_pk_f16_f32 v225, v124, v125
	ds_write_b64 v217, v[224:225] offset:16384
	v_pk_fma_f32 v[118:119], v[118:119], v[220:221], v[18:19]
	v_pk_fma_f32 v[120:121], v[120:121], v[220:221], v[20:21]
	v_max_f32_e32 v118, 0, v118
	v_max_f32_e32 v119, 0, v119
	v_max_f32_e32 v120, 0, v120
	v_max_f32_e32 v121, 0, v121
	v_cvt_pk_f16_f32 v222, v118, v119
	v_cvt_pk_f16_f32 v223, v120, v121
	ds_write_b64 v216, v[222:223] offset:20480
	v_pk_fma_f32 v[114:115], v[114:115], v[220:221], v[10:11]
	v_pk_fma_f32 v[116:117], v[116:117], v[220:221], v[12:13]
	v_max_f32_e32 v114, 0, v114
	v_max_f32_e32 v115, 0, v115
	v_max_f32_e32 v116, 0, v116
	v_max_f32_e32 v117, 0, v117
	v_cvt_pk_f16_f32 v224, v114, v115
	v_cvt_pk_f16_f32 v225, v116, v117
	ds_write_b64 v217, v[224:225] offset:20480
	v_pk_fma_f32 v[110:111], v[110:111], v[220:221], v[34:35]
	v_pk_fma_f32 v[112:113], v[112:113], v[220:221], v[36:37]
	v_max_f32_e32 v110, 0, v110
	v_max_f32_e32 v111, 0, v111
	v_max_f32_e32 v112, 0, v112
	v_max_f32_e32 v113, 0, v113
	v_cvt_pk_f16_f32 v222, v110, v111
	v_cvt_pk_f16_f32 v223, v112, v113
	ds_write_b64 v216, v[222:223] offset:32768
	v_pk_fma_f32 v[106:107], v[106:107], v[220:221], v[26:27]
	v_pk_fma_f32 v[108:109], v[108:109], v[220:221], v[28:29]
	v_max_f32_e32 v106, 0, v106
	v_max_f32_e32 v107, 0, v107
	v_max_f32_e32 v108, 0, v108
	v_max_f32_e32 v109, 0, v109
	v_cvt_pk_f16_f32 v224, v106, v107
	v_cvt_pk_f16_f32 v225, v108, v109
	ds_write_b64 v217, v[224:225] offset:32768
	v_pk_fma_f32 v[102:103], v[102:103], v[220:221], v[18:19]
	v_pk_fma_f32 v[104:105], v[104:105], v[220:221], v[20:21]
	v_max_f32_e32 v102, 0, v102
	v_max_f32_e32 v103, 0, v103
	v_max_f32_e32 v104, 0, v104
	v_max_f32_e32 v105, 0, v105
	v_cvt_pk_f16_f32 v222, v102, v103
	v_cvt_pk_f16_f32 v223, v104, v105
	ds_write_b64 v216, v[222:223] offset:36864
	v_pk_fma_f32 v[98:99], v[98:99], v[220:221], v[10:11]
	v_pk_fma_f32 v[100:101], v[100:101], v[220:221], v[12:13]
	v_max_f32_e32 v98, 0, v98
	v_max_f32_e32 v99, 0, v99
	v_max_f32_e32 v100, 0, v100
	v_max_f32_e32 v101, 0, v101
	v_cvt_pk_f16_f32 v224, v98, v99
	v_cvt_pk_f16_f32 v225, v100, v101
	ds_write_b64 v217, v[224:225] offset:36864
	v_pk_fma_f32 v[94:95], v[94:95], v[220:221], v[34:35]
	v_pk_fma_f32 v[96:97], v[96:97], v[220:221], v[36:37]
	v_max_f32_e32 v94, 0, v94
	v_max_f32_e32 v95, 0, v95
	v_max_f32_e32 v96, 0, v96
	v_max_f32_e32 v97, 0, v97
	v_cvt_pk_f16_f32 v222, v94, v95
	v_cvt_pk_f16_f32 v223, v96, v97
	ds_write_b64 v216, v[222:223] offset:49152
	v_pk_fma_f32 v[90:91], v[90:91], v[220:221], v[26:27]
	v_pk_fma_f32 v[92:93], v[92:93], v[220:221], v[28:29]
	v_max_f32_e32 v90, 0, v90
	v_max_f32_e32 v91, 0, v91
	v_max_f32_e32 v92, 0, v92
	v_max_f32_e32 v93, 0, v93
	v_cvt_pk_f16_f32 v224, v90, v91
	v_cvt_pk_f16_f32 v225, v92, v93
	ds_write_b64 v217, v[224:225] offset:49152
	v_pk_fma_f32 v[86:87], v[86:87], v[220:221], v[18:19]
	v_pk_fma_f32 v[88:89], v[88:89], v[220:221], v[20:21]
	v_max_f32_e32 v86, 0, v86
	v_max_f32_e32 v87, 0, v87
	v_max_f32_e32 v88, 0, v88
	v_max_f32_e32 v89, 0, v89
	v_cvt_pk_f16_f32 v222, v86, v87
	v_cvt_pk_f16_f32 v223, v88, v89
	ds_write_b64 v216, v[222:223] offset:53248
	v_pk_fma_f32 v[82:83], v[82:83], v[220:221], v[10:11]
	v_pk_fma_f32 v[84:85], v[84:85], v[220:221], v[12:13]
	v_max_f32_e32 v82, 0, v82
	v_max_f32_e32 v83, 0, v83
	v_max_f32_e32 v84, 0, v84
	v_max_f32_e32 v85, 0, v85
	v_cvt_pk_f16_f32 v224, v82, v83
	v_cvt_pk_f16_f32 v225, v84, v85
	ds_write_b64 v217, v[224:225] offset:53248
	v_pk_fma_f32 v[78:79], v[78:79], v[220:221], v[34:35]
	v_pk_fma_f32 v[80:81], v[80:81], v[220:221], v[36:37]
	v_max_f32_e32 v78, 0, v78
	v_max_f32_e32 v79, 0, v79
	v_max_f32_e32 v80, 0, v80
	v_max_f32_e32 v81, 0, v81
	v_cvt_pk_f16_f32 v222, v78, v79
	v_cvt_pk_f16_f32 v223, v80, v81
	s_add_u32 s96, s28, 0x0
	s_addc_u32 s97, s29, 0
	global_store_dwordx2 v218, v[222:223], s[96:97] sc1
	v_pk_fma_f32 v[74:75], v[74:75], v[220:221], v[26:27]
	v_pk_fma_f32 v[76:77], v[76:77], v[220:221], v[28:29]
	v_max_f32_e32 v74, 0, v74
	v_max_f32_e32 v75, 0, v75
	v_max_f32_e32 v76, 0, v76
	v_max_f32_e32 v77, 0, v77
	v_cvt_pk_f16_f32 v224, v74, v75
	v_cvt_pk_f16_f32 v225, v76, v77
	global_store_dwordx2 v219, v[224:225], s[96:97] sc1
	v_pk_fma_f32 v[70:71], v[70:71], v[220:221], v[18:19]
	v_pk_fma_f32 v[72:73], v[72:73], v[220:221], v[20:21]
	v_max_f32_e32 v70, 0, v70
	v_max_f32_e32 v71, 0, v71
	v_max_f32_e32 v72, 0, v72
	v_max_f32_e32 v73, 0, v73
	v_cvt_pk_f16_f32 v222, v70, v71
	v_cvt_pk_f16_f32 v223, v72, v73
	s_add_u32 s96, s28, 0x1000
	s_addc_u32 s97, s29, 0
	global_store_dwordx2 v218, v[222:223], s[96:97] sc1
	v_pk_fma_f32 v[66:67], v[66:67], v[220:221], v[10:11]
	v_pk_fma_f32 v[68:69], v[68:69], v[220:221], v[12:13]
	v_max_f32_e32 v66, 0, v66
	v_max_f32_e32 v67, 0, v67
	v_max_f32_e32 v68, 0, v68
	v_max_f32_e32 v69, 0, v69
	v_cvt_pk_f16_f32 v224, v66, v67
	v_cvt_pk_f16_f32 v225, v68, v69
	global_store_dwordx2 v219, v[224:225], s[96:97] sc1
	v_pk_fma_f32 v[62:63], v[62:63], v[220:221], v[34:35]
	v_pk_fma_f32 v[64:65], v[64:65], v[220:221], v[36:37]
	v_max_f32_e32 v62, 0, v62
	v_max_f32_e32 v63, 0, v63
	v_max_f32_e32 v64, 0, v64
	v_max_f32_e32 v65, 0, v65
	v_cvt_pk_f16_f32 v222, v62, v63
	v_cvt_pk_f16_f32 v223, v64, v65
	s_add_u32 s96, s28, 0x2000
	s_addc_u32 s97, s29, 0
	global_store_dwordx2 v218, v[222:223], s[96:97] sc1
	v_pk_fma_f32 v[58:59], v[58:59], v[220:221], v[26:27]
	v_pk_fma_f32 v[60:61], v[60:61], v[220:221], v[28:29]
	v_max_f32_e32 v58, 0, v58
	v_max_f32_e32 v59, 0, v59
	v_max_f32_e32 v60, 0, v60
	v_max_f32_e32 v61, 0, v61
	v_cvt_pk_f16_f32 v224, v58, v59
	v_cvt_pk_f16_f32 v225, v60, v61
	global_store_dwordx2 v219, v[224:225], s[96:97] sc1
	v_pk_fma_f32 v[54:55], v[54:55], v[220:221], v[18:19]
	v_pk_fma_f32 v[56:57], v[56:57], v[220:221], v[20:21]
	v_max_f32_e32 v54, 0, v54
	v_max_f32_e32 v55, 0, v55
	v_max_f32_e32 v56, 0, v56
	v_max_f32_e32 v57, 0, v57
	v_cvt_pk_f16_f32 v222, v54, v55
	v_cvt_pk_f16_f32 v223, v56, v57
	s_add_u32 s96, s28, 0x3000
	s_addc_u32 s97, s29, 0
	global_store_dwordx2 v218, v[222:223], s[96:97] sc1
	v_pk_fma_f32 v[50:51], v[50:51], v[220:221], v[10:11]
	v_pk_fma_f32 v[52:53], v[52:53], v[220:221], v[12:13]
	v_max_f32_e32 v50, 0, v50
	v_max_f32_e32 v51, 0, v51
	v_max_f32_e32 v52, 0, v52
	v_max_f32_e32 v53, 0, v53
	v_cvt_pk_f16_f32 v224, v50, v51
	v_cvt_pk_f16_f32 v225, v52, v53
	global_store_dwordx2 v219, v[224:225], s[96:97] sc1
	v_pk_fma_f32 v[46:47], v[46:47], v[220:221], v[34:35]
	v_pk_fma_f32 v[48:49], v[48:49], v[220:221], v[36:37]
	v_max_f32_e32 v46, 0, v46
	v_max_f32_e32 v47, 0, v47
	v_max_f32_e32 v48, 0, v48
	v_max_f32_e32 v49, 0, v49
	v_cvt_pk_f16_f32 v222, v46, v47
	v_cvt_pk_f16_f32 v223, v48, v49
	s_add_u32 s96, s28, 0x4000
	s_addc_u32 s97, s29, 0
	global_store_dwordx2 v218, v[222:223], s[96:97] sc1
	v_pk_fma_f32 v[42:43], v[42:43], v[220:221], v[26:27]
	v_pk_fma_f32 v[44:45], v[44:45], v[220:221], v[28:29]
	v_max_f32_e32 v42, 0, v42
	v_max_f32_e32 v43, 0, v43
	v_max_f32_e32 v44, 0, v44
	v_max_f32_e32 v45, 0, v45
	v_cvt_pk_f16_f32 v224, v42, v43
	v_cvt_pk_f16_f32 v225, v44, v45
	global_store_dwordx2 v219, v[224:225], s[96:97] sc1
	v_pk_fma_f32 v[38:39], v[38:39], v[220:221], v[18:19]
	v_pk_fma_f32 v[40:41], v[40:41], v[220:221], v[20:21]
	v_max_f32_e32 v38, 0, v38
	v_max_f32_e32 v39, 0, v39
	v_max_f32_e32 v40, 0, v40
	v_max_f32_e32 v41, 0, v41
	v_cvt_pk_f16_f32 v222, v38, v39
	v_cvt_pk_f16_f32 v223, v40, v41
	s_add_u32 s96, s28, 0x5000
	s_addc_u32 s97, s29, 0
	global_store_dwordx2 v218, v[222:223], s[96:97] sc1
	v_pk_fma_f32 v[30:31], v[30:31], v[220:221], v[10:11]
	v_pk_fma_f32 v[32:33], v[32:33], v[220:221], v[12:13]
	v_max_f32_e32 v30, 0, v30
	v_max_f32_e32 v31, 0, v31
	v_max_f32_e32 v32, 0, v32
	v_max_f32_e32 v33, 0, v33
	v_cvt_pk_f16_f32 v224, v30, v31
	v_cvt_pk_f16_f32 v225, v32, v33
	global_store_dwordx2 v219, v[224:225], s[96:97] sc1
	v_pk_fma_f32 v[22:23], v[22:23], v[220:221], v[34:35]
	v_pk_fma_f32 v[24:25], v[24:25], v[220:221], v[36:37]
	v_max_f32_e32 v22, 0, v22
	v_max_f32_e32 v23, 0, v23
	v_max_f32_e32 v24, 0, v24
	v_max_f32_e32 v25, 0, v25
	v_cvt_pk_f16_f32 v222, v22, v23
	v_cvt_pk_f16_f32 v223, v24, v25
	s_add_u32 s96, s28, 0x6000
	s_addc_u32 s97, s29, 0
	global_store_dwordx2 v218, v[222:223], s[96:97] sc1
	v_pk_fma_f32 v[14:15], v[14:15], v[220:221], v[26:27]
	v_pk_fma_f32 v[16:17], v[16:17], v[220:221], v[28:29]
	v_max_f32_e32 v14, 0, v14
	v_max_f32_e32 v15, 0, v15
	v_max_f32_e32 v16, 0, v16
	v_max_f32_e32 v17, 0, v17
	v_cvt_pk_f16_f32 v224, v14, v15
	v_cvt_pk_f16_f32 v225, v16, v17
	global_store_dwordx2 v219, v[224:225], s[96:97] sc1
	v_pk_fma_f32 v[6:7], v[6:7], v[220:221], v[18:19]
	v_pk_fma_f32 v[8:9], v[8:9], v[220:221], v[20:21]
	v_max_f32_e32 v6, 0, v6
	v_max_f32_e32 v7, 0, v7
	v_max_f32_e32 v8, 0, v8
	v_max_f32_e32 v9, 0, v9
	v_cvt_pk_f16_f32 v222, v6, v7
	v_cvt_pk_f16_f32 v223, v8, v9
	s_add_u32 s96, s28, 0x7000
	s_addc_u32 s97, s29, 0
	global_store_dwordx2 v218, v[222:223], s[96:97] sc1
	v_pk_fma_f32 v[2:3], v[2:3], v[220:221], v[10:11]
	v_pk_fma_f32 v[4:5], v[4:5], v[220:221], v[12:13]
	v_max_f32_e32 v2, 0, v2
	v_max_f32_e32 v3, 0, v3
	v_max_f32_e32 v4, 0, v4
	v_max_f32_e32 v5, 0, v5
	v_cvt_pk_f16_f32 v224, v2, v3
	v_cvt_pk_f16_f32 v225, v4, v5
	global_store_dwordx2 v219, v[224:225], s[96:97] sc1
.Lep_done:
	v_and_b32_e32 v189, 63, v0

	.amdhsa_kernel _Z8k_expertPKDF16_S0_PKfPcPiS0_S2_S2_S2_S2_PfS5_S4_S2_S2_S2_S2_S5_S2_S2_S2_
		.amdhsa_group_segment_fixed_size 0
		.amdhsa_private_segment_fixed_size 0
		.amdhsa_kernarg_size 168
		.amdhsa_user_sgpr_count 2
		.amdhsa_user_sgpr_dispatch_ptr 0
		.amdhsa_user_sgpr_queue_ptr 0
		.amdhsa_user_sgpr_kernarg_segment_ptr 1
		.amdhsa_user_sgpr_dispatch_id 0
		.amdhsa_user_sgpr_kernarg_preload_length 0
		.amdhsa_user_sgpr_kernarg_preload_offset 0
		.amdhsa_user_sgpr_private_segment_size 0
		.amdhsa_uses_dynamic_stack 0
		.amdhsa_enable_private_segment 0
		.amdhsa_system_sgpr_workgroup_id_x 1
		.amdhsa_system_sgpr_workgroup_id_y 0
		.amdhsa_system_sgpr_workgroup_id_z 0
		.amdhsa_system_sgpr_workgroup_info 0
		.amdhsa_system_vgpr_workitem_id 0
		.amdhsa_next_free_vgpr 256
		.amdhsa_next_free_sgpr 98
		.amdhsa_accum_offset 256
		.amdhsa_reserve_vcc 1
		.amdhsa_float_round_mode_32 0
		.amdhsa_float_round_mode_16_64 0
		.amdhsa_float_denorm_mode_32 3
		.amdhsa_float_denorm_mode_16_64 3
		.amdhsa_dx10_clamp 1
		.amdhsa_ieee_mode 1
		.amdhsa_fp16_overflow 0
		.amdhsa_tg_split 0
		.amdhsa_exception_fp_ieee_invalid_op 0
		.amdhsa_exception_fp_denorm_src 0
		.amdhsa_exception_fp_ieee_div_zero 0
		.amdhsa_exception_fp_ieee_overflow 0
		.amdhsa_exception_fp_ieee_underflow 0
		.amdhsa_exception_fp_ieee_inexact 0
		.amdhsa_exception_int_div_zero 0
	.end_amdhsa_kernel

amdhsa.kernels:
  - .agpr_count:     0
    .args:
      - .actual_access:  read_only
        .address_space:  global
        .offset:         0
        .size:           8
        .value_kind:     global_buffer
      - .actual_access:  read_only
        .address_space:  global
        .offset:         8
        .size:           8
        .value_kind:     global_buffer
      - .actual_access:  read_only
        .address_space:  global
        .offset:         16
        .size:           8
        .value_kind:     global_buffer
      - .actual_access:  write_only
        .address_space:  global
        .offset:         24
        .size:           8
        .value_kind:     global_buffer
      - .actual_access:  write_only
        .address_space:  global
        .offset:         32
        .size:           8
        .value_kind:     global_buffer
      - .actual_access:  read_only
        .address_space:  global
        .offset:         40
        .size:           8
        .value_kind:     global_buffer
      - .actual_access:  read_only
        .address_space:  global
        .offset:         48
        .size:           8
        .value_kind:     global_buffer
      - .actual_access:  read_only
        .address_space:  global
        .offset:         56
        .size:           8
        .value_kind:     global_buffer
      - .actual_access:  read_only
        .address_space:  global
        .offset:         64
        .size:           8
        .value_kind:     global_buffer
      - .actual_access:  read_only
        .address_space:  global
        .offset:         72
        .size:           8
        .value_kind:     global_buffer
      - .actual_access:  read_only
        .address_space:  global
        .offset:         80
        .size:           8
        .value_kind:     global_buffer
    .group_segment_fixed_size: 16384
    .kernarg_segment_align: 8
    .kernarg_segment_size: 88
    .language:       OpenCL C
    .language_version:
      - 2
      - 0
    .max_flat_workgroup_size: 768
    .name:           _Z9k_router2PKfPKDF16_S0_PDF16_PfPiS0_S0_S4_S5_S4_
    .private_segment_fixed_size: 0
    .sgpr_count:     21
    .sgpr_spill_count: 0
    .symbol:         _Z9k_router2PKfPKDF16_S0_PDF16_PfPiS0_S0_S4_S5_S4_.kd
    .uniform_work_group_size: 1
    .uses_dynamic_stack: false
    .vgpr_count:     168
    .vgpr_spill_count: 0
    .wavefront_size: 64
  - .agpr_count:     0
    .args:
      - .actual_access:  read_only
        .address_space:  global
        .offset:         0
        .size:           8
        .value_kind:     global_buffer
      - .actual_access:  read_only
        .address_space:  global
        .offset:         8
        .size:           8
        .value_kind:     global_buffer
      - .actual_access:  read_only
        .address_space:  global
        .offset:         16
        .size:           8
        .value_kind:     global_buffer
      - .actual_access:  write_only
        .address_space:  global
        .offset:         24
        .size:           8
        .value_kind:     global_buffer
      - .actual_access:  write_only
        .address_space:  global
        .offset:         32
        .size:           8
        .value_kind:     global_buffer
      - .actual_access:  write_only
        .address_space:  global
        .offset:         40
        .size:           8
        .value_kind:     global_buffer
    .group_segment_fixed_size: 256
    .kernarg_segment_align: 8
    .kernarg_segment_size: 48
    .language:       OpenCL C
    .language_version:
      - 2
      - 0
    .max_flat_workgroup_size: 256
    .name:           _Z6k_gatePKfS0_S0_PfPiS1_
    .private_segment_fixed_size: 0
    .sgpr_count:     26
    .sgpr_spill_count: 0
    .symbol:         _Z6k_gatePKfS0_S0_PfPiS1_.kd
    .uniform_work_group_size: 1
    .uses_dynamic_stack: false
    .vgpr_count:     51
    .vgpr_spill_count: 0
    .wavefront_size: 64
  - .agpr_count:     0
    .args:
      - .actual_access:  read_only
        .address_space:  global
        .offset:         0
        .size:           8
        .value_kind:     global_buffer
      - .actual_access:  write_only
        .address_space:  global
        .offset:         8
        .size:           8
        .value_kind:     global_buffer
      - .actual_access:  read_only
        .address_space:  global
        .offset:         16
        .size:           8
        .value_kind:     global_buffer
      - .actual_access:  read_only
        .address_space:  global
        .offset:         24
        .size:           8
        .value_kind:     global_buffer
      - .actual_access:  read_only
        .address_space:  global
        .offset:         32
        .size:           8
        .value_kind:     global_buffer
      - .actual_access:  write_only
        .address_space:  global
        .offset:         40
        .size:           8
        .value_kind:     global_buffer
      - .actual_access:  write_only
        .address_space:  global
        .offset:         48
        .size:           8
        .value_kind:     global_buffer
      - .actual_access:  write_only
        .address_space:  global
        .offset:         56
        .size:           8
        .value_kind:     global_buffer
      - .actual_access:  write_only
        .address_space:  global
        .offset:         64
        .size:           8
        .value_kind:     global_buffer
      - .actual_access:  write_only
        .address_space:  global
        .offset:         72
        .size:           8
        .value_kind:     global_buffer
    .group_segment_fixed_size: 16640
    .kernarg_segment_align: 8
    .kernarg_segment_size: 80
    .language:       OpenCL C
    .language_version:
      - 2
      - 0
    .max_flat_workgroup_size: 256
    .name:           _Z10k_prep_allPKfPDF16_S0_S0_S0_S1_S1_PiS2_S2_
    .private_segment_fixed_size: 0
    .sgpr_count:     20
    .sgpr_spill_count: 0
    .symbol:         _Z10k_prep_allPKfPDF16_S0_S0_S0_S1_S1_PiS2_S2_.kd
    .uniform_work_group_size: 1
    .uses_dynamic_stack: false
    .vgpr_count:     37
    .vgpr_spill_count: 0
    .wavefront_size: 64
  - .agpr_count:     0
    .args:
      - .address_space:  global
        .offset:         0
        .size:           8
        .value_kind:     global_buffer
      - .address_space:  global
        .offset:         8
        .size:           8
        .value_kind:     global_buffer
      - .actual_access:  read_only
        .address_space:  global
        .offset:         16
        .size:           8
        .value_kind:     global_buffer
      - .actual_access:  read_only
        .address_space:  global
        .offset:         24
        .size:           8
        .value_kind:     global_buffer
      - .actual_access:  write_only
        .address_space:  global
        .offset:         32
        .size:           8
        .value_kind:     global_buffer
    .group_segment_fixed_size: 0
    .kernarg_segment_align: 8
    .kernarg_segment_size: 40
    .language:       OpenCL C
    .language_version:
      - 2
      - 0
    .max_flat_workgroup_size: 512
    .name:           _Z7k_gemm1PKDF16_S0_PKfPKiPDF16_
    .private_segment_fixed_size: 0
    .sgpr_count:     36
    .sgpr_spill_count: 0
    .symbol:         _Z7k_gemm1PKDF16_S0_PKfPKiPDF16_.kd
    .uniform_work_group_size: 1
    .uses_dynamic_stack: false
    .vgpr_count:     240
    .vgpr_spill_count: 0
    .wavefront_size: 64
  - .agpr_count:     0
    .args:
      - .address_space:  global
        .offset:         0
        .size:           8
        .value_kind:     global_buffer
      - .actual_access:  read_only
        .address_space:  global
        .offset:         8
        .size:           8
        .value_kind:     global_buffer
      - .actual_access:  read_only
        .address_space:  global
        .offset:         16
        .size:           8
        .value_kind:     global_buffer
      - .actual_access:  read_only
        .address_space:  global
        .offset:         24
        .size:           8
        .value_kind:     global_buffer
      - .actual_access:  read_only
        .address_space:  global
        .offset:         32
        .size:           8
        .value_kind:     global_buffer
      - .actual_access:  read_only
        .address_space:  global
        .offset:         40
        .size:           8
        .value_kind:     global_buffer
      - .actual_access:  read_only
        .address_space:  global
        .offset:         48
        .size:           8
        .value_kind:     global_buffer
      - .actual_access:  write_only
        .address_space:  global
        .offset:         56
        .size:           8
        .value_kind:     global_buffer
      - .actual_access:  write_only
        .address_space:  global
        .offset:         64
        .size:           8
        .value_kind:     global_buffer
    .group_segment_fixed_size: 0
    .kernarg_segment_align: 8
    .kernarg_segment_size: 72
    .language:       OpenCL C
    .language_version:
      - 2
      - 0
    .max_flat_workgroup_size: 512
    .name:           _Z11k_gemm2poolPKDF16_S0_PKfS2_S2_S2_PKiPfS5_
    .private_segment_fixed_size: 0
    .sgpr_count:     32
    .sgpr_spill_count: 0
    .symbol:         _Z11k_gemm2poolPKDF16_S0_PKfS2_S2_S2_PKiPfS5_.kd
    .uniform_work_group_size: 1
    .uses_dynamic_stack: false
    .vgpr_count:     198
    .vgpr_spill_count: 0
    .wavefront_size: 64
  - .agpr_count:     0
    .args:
      - .address_space:  global
        .offset:         0
        .size:           8
        .value_kind:     global_buffer
      - .address_space:  global
        .offset:         8
        .size:           8
        .value_kind:     global_buffer
      - .actual_access:  read_only
        .address_space:  global
        .offset:         16
        .size:           8
        .value_kind:     global_buffer
      - .address_space:  global
        .offset:         24
        .size:           8
        .value_kind:     global_buffer
      - .address_space:  global
        .offset:         32
        .size:           8
        .value_kind:     global_buffer
      - .actual_access:  read_only
        .address_space:  global
        .offset:         40
        .size:           8
        .value_kind:     global_buffer
      - .actual_access:  read_only
        .address_space:  global
        .offset:         48
        .size:           8
        .value_kind:     global_buffer
      - .actual_access:  read_only
        .address_space:  global
        .offset:         56
        .size:           8
        .value_kind:     global_buffer
      - .actual_access:  read_only
        .address_space:  global
        .offset:         64
        .size:           8
        .value_kind:     global_buffer
      - .actual_access:  read_only
        .address_space:  global
        .offset:         72
        .size:           8
        .value_kind:     global_buffer
      - .address_space:  global
        .offset:         80
        .size:           8
        .value_kind:     global_buffer
      - .address_space:  global
        .offset:         88
        .size:           8
        .value_kind:     global_buffer
      - .address_space:  global
        .offset:         96
        .size:           8
        .value_kind:     global_buffer
      - .actual_access:  read_only
        .address_space:  global
        .offset:         104
        .size:           8
        .value_kind:     global_buffer
      - .actual_access:  read_only
        .address_space:  global
        .offset:         112
        .size:           8
        .value_kind:     global_buffer
      - .actual_access:  read_only
        .address_space:  global
        .offset:         120
        .size:           8
        .value_kind:     global_buffer
      - .actual_access:  read_only
        .address_space:  global
        .offset:         128
        .size:           8
        .value_kind:     global_buffer
      - .actual_access:  write_only
        .address_space:  global
        .offset:         136
        .size:           8
        .value_kind:     global_buffer
      - .actual_access:  read_only
        .address_space:  global
        .offset:         144
        .size:           8
        .value_kind:     global_buffer
      - .actual_access:  read_only
        .address_space:  global
        .offset:         152
        .size:           8
        .value_kind:     global_buffer
      - .actual_access:  read_only
        .address_space:  global
        .offset:         160
        .size:           8
        .value_kind:     global_buffer
    .group_segment_fixed_size: 0
    .kernarg_segment_align: 8
    .kernarg_segment_size: 168
    .language:       OpenCL C
    .language_version:
      - 2
      - 0
    .max_flat_workgroup_size: 512
    .name:           _Z8k_expertPKDF16_S0_PKfPcPiS0_S2_S2_S2_S2_PfS5_S4_S2_S2_S2_S2_S5_S2_S2_S2_
    .private_segment_fixed_size: 0
    .sgpr_count:     104
    .sgpr_spill_count: 0
    .symbol:         _Z8k_expertPKDF16_S0_PKfPcPiS0_S2_S2_S2_S2_PfS5_S4_S2_S2_S2_S2_S5_S2_S2_S2_.kd
    .uniform_work_group_size: 1
    .uses_dynamic_stack: false
    .vgpr_count:     256
    .vgpr_spill_count: 0
    .wavefront_size: 64
  - .agpr_count:     0
    .args:
      - .actual_access:  read_only
        .address_space:  global
        .offset:         0
        .size:           8
        .value_kind:     global_buffer
      - .actual_access:  read_only
        .address_space:  global
        .offset:         8
        .size:           8
        .value_kind:     global_buffer
      - .actual_access:  read_only
        .address_space:  global
        .offset:         16
        .size:           8
        .value_kind:     global_buffer
      - .actual_access:  read_only
        .address_space:  global
        .offset:         24
        .size:           8
        .value_kind:     global_buffer
      - .actual_access:  read_only
        .address_space:  global
        .offset:         32
        .size:           8
        .value_kind:     global_buffer
      - .actual_access:  read_only
        .address_space:  global
        .offset:         40
        .size:           8
        .value_kind:     global_buffer
      - .actual_access:  read_only
        .address_space:  global
        .offset:         48
        .size:           8
        .value_kind:     global_buffer
      - .actual_access:  read_only
        .address_space:  global
        .offset:         56
        .size:           8
        .value_kind:     global_buffer
      - .actual_access:  write_only
        .address_space:  global
        .offset:         64
        .size:           8
        .value_kind:     global_buffer
    .group_segment_fixed_size: 8768
    .kernarg_segment_align: 8
    .kernarg_segment_size: 72
    .language:       OpenCL C
    .language_version:
      - 2
      - 0
    .max_flat_workgroup_size: 1024
    .name:           _Z7k_finalPKfS0_S0_S0_S0_PKiS0_S0_Pf
    .private_segment_fixed_size: 0
    .sgpr_count:     24
    .sgpr_spill_count: 0
    .symbol:         _Z7k_finalPKfS0_S0_S0_S0_PKiS0_S0_Pf.kd
    .uniform_work_group_size: 1
    .uses_dynamic_stack: false
    .vgpr_count:     83
    .vgpr_spill_count: 0
    .wavefront_size: 64
